# baseline (speedup 1.0000x reference)
.Lrec_loop:
	s_add_i32 s10, s36, -1
	s_and_b32 s54, s10, 1
	v_lshl_add_u32 v164, s54, 18, v186
	s_bfe_u32 s54, s10, 0x10001
	s_mul_i32 s54, s54, 0x40004000
	s_sleep 10
	buffer_load_dwordx4 v[16:19], v164, s[16:19], 0 offen sc1
	buffer_load_dwordx4 v[20:23], v164, s[16:19], 0 offen offset:1024 sc1
	buffer_load_dwordx4 v[24:27], v164, s[16:19], 0 offen offset:2048 sc1
	buffer_load_dwordx4 v[28:31], v164, s[16:19], 0 offen offset:3072 sc1
	s_lshl_b32 s41, s36, 7
	s_mov_b32 s43, 0
	s_mov_b32 s45, 15
	s_mov_b32 s46, 0
	s_mov_b32 s55, 0
	s_add_i32 s11, s41, 0x80
	v_add_u32_e32 v206, s11, v169
	v_mov_b32_e32 v207, 0
	v_lshlrev_b64 v[206:207], 14, v[206:207]
	v_lshl_add_u64 v[206:207], v[174:175], 0, v[206:207]
	s_lshl_b32 s11, s36, 16
	s_and_b32 s11, s11, 0x10000
	v_add_u32_e32 v173, s11, v170
	s_waitcnt vmcnt(3)
	v_xor_b32_e32 v16, s54, v16
	v_xor_b32_e32 v17, s54, v17
	v_xor_b32_e32 v18, s54, v18
	v_xor_b32_e32 v19, s54, v19
	v_or3_b32 v0, v16, v17, v18
	v_bitop3_b32 v0, v0, s39, v19 bitop3:0xc8
	v_cmp_ne_u32_e32 vcc, 0, v0
	s_cmp_lg_u64 vcc, 0
	s_cbranch_scc1 .Lrec_e0dirty
	s_bitset0_b32 s45, 0
	v_mfma_f32_16x16x32_f16 v[198:201], v[152:155], v[16:19], 0
	v_mfma_f32_16x16x32_f16 v[202:205], v[48:51], v[16:19], 0
	v_mfma_f32_16x16x32_f16 v[212:215], v[88:91], v[16:19], 0
	v_mfma_f32_16x16x32_f16 v[216:219], v[92:95], v[16:19], 0
	v_mfma_f32_16x16x32_f16 v[220:223], v[108:111], v[16:19], 0
	v_mfma_f32_16x16x32_f16 v[224:227], v[112:115], v[16:19], 0
	v_mfma_f32_16x16x32_f16 v[228:231], v[140:143], v[16:19], 0
	v_mfma_f32_16x16x32_f16 v[232:235], v[32:35], v[16:19], v[160:163]
	s_mov_b32 s46, 1
	s_waitcnt vmcnt(2)
	v_xor_b32_e32 v20, s54, v20
	v_xor_b32_e32 v21, s54, v21
	v_xor_b32_e32 v22, s54, v22
	v_xor_b32_e32 v23, s54, v23
	v_or3_b32 v0, v20, v21, v22
	v_bitop3_b32 v0, v0, s39, v23 bitop3:0xc8
	v_cmp_ne_u32_e32 vcc, 0, v0
	s_cmp_lg_u64 vcc, 0
	s_cbranch_scc1 .Lrec_e1dirty
	s_bitset0_b32 s45, 1
	v_mfma_f32_16x16x32_f16 v[198:201], v[52:55], v[20:23], v[198:201]
	v_mfma_f32_16x16x32_f16 v[202:205], v[56:59], v[20:23], v[202:205]
	v_mfma_f32_16x16x32_f16 v[212:215], v[76:79], v[20:23], v[212:215]
	v_mfma_f32_16x16x32_f16 v[216:219], v[96:99], v[20:23], v[216:219]
	v_mfma_f32_16x16x32_f16 v[220:223], v[116:119], v[20:23], v[220:223]
	v_mfma_f32_16x16x32_f16 v[224:227], v[120:123], v[20:23], v[224:227]
	v_mfma_f32_16x16x32_f16 v[228:231], v[144:147], v[20:23], v[228:231]
	v_mfma_f32_16x16x32_f16 v[232:235], v[36:39], v[20:23], v[232:235]
	s_mov_b32 s46, 2
	s_waitcnt vmcnt(1)
	v_xor_b32_e32 v24, s54, v24
	v_xor_b32_e32 v25, s54, v25
	v_xor_b32_e32 v26, s54, v26
	v_xor_b32_e32 v27, s54, v27
	v_or3_b32 v0, v24, v25, v26
	v_bitop3_b32 v0, v0, s39, v27 bitop3:0xc8
	v_cmp_ne_u32_e32 vcc, 0, v0
	s_cmp_lg_u64 vcc, 0
	s_cbranch_scc1 .Lrec_e2dirty
	s_bitset0_b32 s45, 2
	v_mfma_f32_16x16x32_f16 v[198:201], v[60:63], v[24:27], v[198:201]
	v_mfma_f32_16x16x32_f16 v[202:205], v[64:67], v[24:27], v[202:205]
	v_mfma_f32_16x16x32_f16 v[212:215], v[80:83], v[24:27], v[212:215]
	v_mfma_f32_16x16x32_f16 v[216:219], v[100:103], v[24:27], v[216:219]
	v_mfma_f32_16x16x32_f16 v[220:223], v[124:127], v[24:27], v[220:223]
	v_mfma_f32_16x16x32_f16 v[224:227], v[128:131], v[24:27], v[224:227]
	v_mfma_f32_16x16x32_f16 v[228:231], v[148:151], v[24:27], v[228:231]
	v_mfma_f32_16x16x32_f16 v[232:235], v[40:43], v[24:27], v[232:235]
	s_mov_b32 s46, 3
	s_branch .Lrec_wait
.Lrec_e0dirty:
	buffer_load_dwordx4 v[16:19], v164, s[16:19], 0 offen sc1
	s_branch .Lrec_wait
.Lrec_e1dirty:
	buffer_load_dwordx4 v[20:23], v164, s[16:19], 0 offen offset:1024 sc1
	s_branch .Lrec_wait
.Lrec_e2dirty:
	buffer_load_dwordx4 v[24:27], v164, s[16:19], 0 offen offset:2048 sc1
.Lrec_wait:
	s_waitcnt vmcnt(0)
